# v51 + indexer bitmask-word stores non-temporal (no L2 pollution by the scattered words)
# baseline (speedup 1.0000x reference)
.LBB0_1975:
	s_lshl_b32 s80, s0, 23
	v_lshl_add_u64 v[2:3], v[106:107], 0, s[80:81]
	s_lshl_b32 s80, s34, 2
	s_or_b32 s29, s1, 7
	v_lshl_add_u64 v[2:3], v[2:3], 0, s[80:81]
	s_mov_b32 s65, s81
	v_readlane_b32 s91, v253, 27
	v_readlane_b32 s92, v253, 28
	s_mov_b32 s89, 0x2e8ba2e9
	s_movk_i32 s95, 0x100
	s_movk_i32 s90, 0xfea0
	s_movk_i32 s94, 0x2000
	v_lshl_add_u64 v[2:3], v[2:3], 0, s[64:65]
	v_cmp_ge_i32_e32 vcc, s29, v104
	v_readlane_b32 s93, v253, 29
	s_and_saveexec_b64 s[42:43], vcc
	s_cbranch_execz .LBB0_1977
	global_store_dword v[2:3], v0, off nt
.LBB0_1977:
	s_or_b64 exec, exec, s[42:43]
	v_cmp_ge_i32_e32 vcc, s29, v105
	s_and_saveexec_b64 s[42:43], vcc
	s_cbranch_execz .LBB0_1979
	v_add_co_u32_e32 v2, vcc, 0x400000, v2
	s_nop 1
	v_addc_co_u32_e32 v3, vcc, 0, v3, vcc
	global_store_dword v[2:3], v4, off nt
